# in-proj and gate_up: accumulator zeroing (128 v_mov per unit) removed; first K-loop iteration peeled with srcC = 0 on each accumulator's first MFMA; on top of the three epilogue rewrites
# speedup vs baseline: 1.0183x; 1.0012x over previous
;     __device__ __forceinline__ void a_ready(const Unit&) const { if (++ncall == 3 && sig != nullptr && threadIdx.x == 0) __hip_atomic_fetch_add(sig, 1u, __ATOMIC_RELAXED, __HIP_MEMORY_SCOPE_AGENT); }
;     __device__ bool next(int i, Unit& u) const { if (!base.next(i >> 1, u)) return false; if (i & 1) { u.pm += MTOK / BM; u.pn += DM / BM; } return true; }
; #define PG8_WAIT_V(n) asm volatile("s_waitcnt vmcnt(" #n ")" ::: "memory")
; template <class Epi, class Sched, bool ALIGN_EPI = false, bool SP2 = false>
; __device__ __forceinline__ void gemm_phase(PG8_LAS unsigned char* lds, const Gemm g, const Sched& S, const Epi& E) {
;     ...
;     for (;;) {
;         const bool has_next = S.next(ui + 1, nxt);
;         const char* nA = has_next ? (const char*)g.A + (size_t)nxt.pm * tstep + (nxt.half == 2 ? hstep : (size_t)0) : cA; const char* nB = has_next ? (const char*)g.Bt + (size_t)nxt.pn * tstep : cB;
;         for (int t = 0; t < nt; t += 2) {
;             const bool last = (t == nt - 2);
;             const char* a1 = cA + (size_t)(t + 1) * kstep;
;             const char* a2 = last ? nA : cA + (size_t)(t + 2) * kstep; const char* b2 = last ? nB : cB + (size_t)(t + 2) * kstep;
;             const char* a3 = a2 + kstep; const char* b3 = b2 + kstep;
;             if (last && has_next) S.a_ready(nxt);
;             if constexpr (SP2) {
;             PG8_LDB(B0, 0, 0); PG8_LDB(B1, 0, 1); PG8_SCHED; PG8_LDA(At, 0, 0); PG8_STAGE(PG8_SA(1, 1), a1 + hstep, voffA);
;     ...
;             if (PROBE_KIND == 18 && t == 0 && ui > 0 && g.probe) { const unsigned long long tq_ = __builtin_amdgcn_s_memrealtime(); PG8_WAIT_V(8); pg8_probe_acc += (unsigned)(__builtin_amdgcn_s_memrealtime() - tq_); }
;     ...
;             PG8_WAIT_V(8); PG8_WAIT_L(0); PG8_BAR; PG8_MMA(0, 0, At, B0); PG8_MMA(0, 1, At, B1); PG8_BAR; PG8_SCHED;
;             PG8_LDA(At, 0, 1); PG8_STAGE(PG8_SB(0, 0), b2, voffB); PG8_STAGE(PG8_SB(0, 1), b2 + hstep, voffB); PG8_STAGE(PG8_SA(0, 0), a2, voffA);
;             PG8_WAIT_V(8); PG8_WAIT_L(0); PG8_BAR; if (cur.half == 0) { PG8_MMA(1, 0, At, B0); PG8_MMA(1, 1, At, B1); } PG8_BAR; PG8_SCHED;
;     ...
;         for (int a = 0; a < 2; ++a)
; #pragma unroll
;             for (int b = 0; b < 2; ++b)
; #pragma unroll
;                 for (int m = 0; m < 4; ++m)
; #pragma unroll
;                     for (int n = 0; n < 2; ++n) acc[a][b][m][n] = (f32x4){0.f, 0.f, 0.f, 0.f};
.LBB0_394:
	s_ashr_i32 s61, s60, 31
	s_lshl_b64 s[10:11], s[60:61], 19
	s_add_u32 s66, s24, s10
	s_addc_u32 s67, s25, s11
	s_and_b64 s[10:11], s[64:65], exec
	s_cselect_b32 s12, s67, s9
	s_cselect_b32 s13, s66, s8
	s_ashr_i32 s63, s62, 31
	s_lshl_b64 s[10:11], s[62:63], 19
	s_add_u32 s68, s28, s10
	s_addc_u32 s69, s29, s11
	s_and_b64 s[10:11], s[64:65], exec
	s_cselect_b32 s14, s69, s1
	s_cselect_b32 s15, s68, s0
	s_add_u32 s8, s8, 0x40080
	s_addc_u32 s9, s9, 0
	s_add_u32 s36, s0, 0x100
	s_addc_u32 s38, s1, 0
	s_mov_b32 s39, -2
	s_waitcnt lgkmcnt(0)
	s_add_u32 s0, s8, 0xfffc0080
	s_addc_u32 s1, s9, -1
	s_add_i32 s61, 0, 0x10000
	s_cmp_eq_u32 s39, 12
	s_cselect_b32 s11, s12, s1
	s_cselect_b32 s10, s13, s0
	v_add_u32_e32 v2, s61, v203
	s_cselect_b32 s1, s14, s38
	s_cselect_b32 s0, s15, s36
	s_add_i32 s63, 0, 0x14000
	ds_read_b128 v[132:135], v2
	ds_read_b128 v[136:139], v2 offset:1024
	ds_read_b128 v[140:143], v2 offset:2048
	ds_read_b128 v[144:147], v2 offset:3072
	v_add_u32_e32 v2, s63, v203
	ds_read_b128 v[148:151], v2
	ds_read_b128 v[152:155], v2 offset:1024
	ds_read_b128 v[156:159], v2 offset:2048
	ds_read_b128 v[160:163], v2 offset:3072
	v_lshl_add_u64 v[228:229], s[8:9], 0, v[178:179]
	s_add_i32 m0, s19, 0xc000
	ds_read_b128 v[182:185], v206
	ds_read_b128 v[186:189], v206 offset:1024
	ds_read_b128 v[190:193], v206 offset:2048
	ds_read_b128 v[194:197], v206 offset:3072
	ds_read_b128 v[198:201], v206 offset:4096
	ds_read_b128 v[208:211], v206 offset:5120
	ds_read_b128 v[212:215], v206 offset:6144
	ds_read_b128 v[216:219], v206 offset:7168
	global_load_lds_dwordx4 v[228:229], off
	v_lshl_add_u64 v[228:229], s[8:9], 0, v[180:181]
	s_add_i32 m0, s19, 0xe000
	s_nop 0
	global_load_lds_dwordx4 v[228:229], off
	s_waitcnt vmcnt(8)
	s_waitcnt lgkmcnt(0)
	s_barrier
	s_setprio 1
	s_waitcnt lgkmcnt(0)
	v_mfma_f32_16x16x32_bf16 v[128:131], v[132:135], v[182:185], 0
	v_mfma_f32_16x16x32_bf16 v[124:127], v[140:143], v[182:185], 0
	v_mfma_f32_16x16x32_bf16 v[112:115], v[132:135], v[190:193], 0
	v_mfma_f32_16x16x32_bf16 v[108:111], v[140:143], v[190:193], 0
	v_mfma_f32_16x16x32_bf16 v[96:99], v[132:135], v[198:201], 0
	v_mfma_f32_16x16x32_bf16 v[92:95], v[140:143], v[198:201], 0
	v_mfma_f32_16x16x32_bf16 v[80:83], v[132:135], v[212:215], 0
	v_mfma_f32_16x16x32_bf16 v[76:79], v[140:143], v[212:215], 0
	v_mfma_f32_16x16x32_bf16 v[128:131], v[136:139], v[186:189], v[128:131]
	v_mfma_f32_16x16x32_bf16 v[124:127], v[144:147], v[186:189], v[124:127]
	v_mfma_f32_16x16x32_bf16 v[112:115], v[136:139], v[194:197], v[112:115]
	v_mfma_f32_16x16x32_bf16 v[108:111], v[144:147], v[194:197], v[108:111]
	v_mfma_f32_16x16x32_bf16 v[96:99], v[136:139], v[208:211], v[96:99]
	v_mfma_f32_16x16x32_bf16 v[92:95], v[144:147], v[208:211], v[92:95]
	v_mfma_f32_16x16x32_bf16 v[80:83], v[136:139], v[216:219], v[80:83]
	v_mfma_f32_16x16x32_bf16 v[76:79], v[144:147], v[216:219], v[76:79]
	s_setprio 0
	s_setprio 1
	v_mfma_f32_16x16x32_bf16 v[120:123], v[148:151], v[182:185], 0
	v_mfma_f32_16x16x32_bf16 v[116:119], v[156:159], v[182:185], 0
	v_mfma_f32_16x16x32_bf16 v[104:107], v[148:151], v[190:193], 0
	v_mfma_f32_16x16x32_bf16 v[100:103], v[156:159], v[190:193], 0
	v_mfma_f32_16x16x32_bf16 v[88:91], v[148:151], v[198:201], 0
	v_mfma_f32_16x16x32_bf16 v[84:87], v[156:159], v[198:201], 0
	v_mfma_f32_16x16x32_bf16 v[72:75], v[148:151], v[212:215], 0
	v_mfma_f32_16x16x32_bf16 v[68:71], v[156:159], v[212:215], 0
	v_mfma_f32_16x16x32_bf16 v[120:123], v[152:155], v[186:189], v[120:123]
	v_mfma_f32_16x16x32_bf16 v[116:119], v[160:163], v[186:189], v[116:119]
	v_mfma_f32_16x16x32_bf16 v[104:107], v[152:155], v[194:197], v[104:107]
	v_mfma_f32_16x16x32_bf16 v[100:103], v[160:163], v[194:197], v[100:103]
	v_mfma_f32_16x16x32_bf16 v[88:91], v[152:155], v[208:211], v[88:91]
	v_mfma_f32_16x16x32_bf16 v[84:87], v[160:163], v[208:211], v[84:87]
	v_mfma_f32_16x16x32_bf16 v[72:75], v[152:155], v[216:219], v[72:75]
	v_mfma_f32_16x16x32_bf16 v[68:71], v[160:163], v[216:219], v[68:71]
	s_setprio 0
	s_barrier
	s_add_i32 s61, s61, s27
	v_lshl_add_u64 v[228:229], s[0:1], 0, v[166:167]
	s_mov_b32 m0, s61
	ds_read_b128 v[182:185], v206 offset:16384
	ds_read_b128 v[186:189], v206 offset:17408
	ds_read_b128 v[190:193], v206 offset:18432
	ds_read_b128 v[194:197], v206 offset:19456
	ds_read_b128 v[198:201], v206 offset:20480
	ds_read_b128 v[208:211], v206 offset:21504
	ds_read_b128 v[212:215], v206 offset:22528
	ds_read_b128 v[216:219], v206 offset:23552
	global_load_lds_dwordx4 v[228:229], off
	s_add_i32 m0, s61, 0x2000
	s_add_u32 s78, s0, 0x40000
	v_lshl_add_u64 v[230:231], s[0:1], 0, v[170:171]
	s_addc_u32 s79, s1, 0
	s_add_i32 s61, s63, s27
	global_load_lds_dwordx4 v[230:231], off
	v_lshl_add_u64 v[232:233], s[78:79], 0, v[166:167]
	s_mov_b32 m0, s61
	v_lshl_add_u64 v[234:235], s[10:11], 0, v[168:169]
	global_load_lds_dwordx4 v[232:233], off
	v_lshl_add_u64 v[232:233], s[78:79], 0, v[170:171]
	s_add_i32 m0, s61, 0x2000
	s_nop 0
	global_load_lds_dwordx4 v[232:233], off
	v_lshl_add_u64 v[232:233], s[10:11], 0, v[164:165]
	s_mov_b32 m0, s19
	s_nop 0
	global_load_lds_dwordx4 v[232:233], off
	s_mov_b32 m0, s30
	s_nop 0
	global_load_lds_dwordx4 v[234:235], off
	s_waitcnt vmcnt(8)
	s_waitcnt lgkmcnt(0)
	s_barrier
; #define PG8_STAGE(bufoff, gbase, voff) do { _Pragma("unroll") for (int _i = 0; _i < 2; ++_i) \
;         __builtin_amdgcn_global_load_lds((const unsigned*)((const char*)(gbase) + (voff)[_i]), (PG8_LAS unsigned*)(lds + (bufoff) + ldsw + _i * 8192), 16, 0, 0); } while (0)
; #define PG8_LDA(dst, b, h) do { _Pragma("unroll") for (int m = 0; m < 4; ++m) _Pragma("unroll") for (int k = 0; k < 2; ++k) dst[m][k] = *(const PG8_LAS bf16x8*)(lds + PG8_SA(b, h) + aoff + m * 2048 + k * 1024); } while (0)
; #define PG8_LDB(dst, b, h) do { _Pragma("unroll") for (int n = 0; n < 2; ++n) _Pragma("unroll") for (int k = 0; k < 2; ++k) dst[n][k] = *(const PG8_LAS bf16x8*)(lds + PG8_SB(b, h) + boff + n * 2048 + k * 1024); } while (0)
; #define PG8_MMA(ai, bj, At, Bt) do { __builtin_amdgcn_s_setprio(1); _Pragma("unroll") for (int m = 0; m < 4; ++m) _Pragma("unroll") for (int n = 0; n < 2; ++n) _Pragma("unroll") for (int k = 0; k < 2; ++k) \
;         acc[ai][bj][m][n] = __builtin_amdgcn_mfma_f32_16x16x32_bf16(Bt[n][k], At[m][k], acc[ai][bj][m][n], 0, 0, 0); __builtin_amdgcn_s_setprio(0); } while (0)
; #define PG8_WAIT_V(n) asm volatile("s_waitcnt vmcnt(" #n ")" ::: "memory")
; #define PG8_WAIT_L(n) asm volatile("s_waitcnt lgkmcnt(" #n ")" ::: "memory")
; #define PG8_BAR __builtin_amdgcn_s_barrier()
; #define PG8_SCHED __builtin_amdgcn_sched_barrier(0)
; template <class Epi, class Sched, bool ALIGN_EPI = false, bool SP2 = false>
; __device__ __forceinline__ void gemm_phase(PG8_LAS unsigned char* lds, const Gemm g, const Sched& S, const Epi& E) {
;     ...
;             PG8_WAIT_V(8); PG8_WAIT_L(0); PG8_BAR; if (cur.half == 0) { PG8_MMA(1, 0, At, B0); PG8_MMA(1, 1, At, B1); } PG8_BAR; PG8_SCHED;
;             PG8_LDB(B0, 1, 0); PG8_LDB(B1, 1, 1); PG8_SCHED; PG8_LDA(At, 1, 0); PG8_STAGE(PG8_SA(0, 1), a2 + hstep, voffA);
;             PG8_WAIT_V(8); PG8_WAIT_L(0); PG8_BAR; PG8_MMA(0, 0, At, B0); PG8_MMA(0, 1, At, B1); PG8_BAR; PG8_SCHED;
	s_setprio 1
	s_waitcnt lgkmcnt(0)
	v_mfma_f32_16x16x32_bf16 v[64:67], v[132:135], v[182:185], 0
	v_mfma_f32_16x16x32_bf16 v[60:63], v[140:143], v[182:185], 0
	v_mfma_f32_16x16x32_bf16 v[48:51], v[132:135], v[190:193], 0
	v_mfma_f32_16x16x32_bf16 v[44:47], v[140:143], v[190:193], 0
	v_mfma_f32_16x16x32_bf16 v[32:35], v[132:135], v[198:201], 0
	v_mfma_f32_16x16x32_bf16 v[28:31], v[140:143], v[198:201], 0
	v_mfma_f32_16x16x32_bf16 v[16:19], v[132:135], v[212:215], 0
	v_mfma_f32_16x16x32_bf16 v[12:15], v[140:143], v[212:215], 0
	v_mfma_f32_16x16x32_bf16 v[64:67], v[136:139], v[186:189], v[64:67]
	v_mfma_f32_16x16x32_bf16 v[60:63], v[144:147], v[186:189], v[60:63]
	v_mfma_f32_16x16x32_bf16 v[48:51], v[136:139], v[194:197], v[48:51]
	v_mfma_f32_16x16x32_bf16 v[44:47], v[144:147], v[194:197], v[44:47]
	v_mfma_f32_16x16x32_bf16 v[32:35], v[136:139], v[208:211], v[32:35]
	v_mfma_f32_16x16x32_bf16 v[28:31], v[144:147], v[208:211], v[28:31]
	v_mfma_f32_16x16x32_bf16 v[16:19], v[136:139], v[216:219], v[16:19]
	v_mfma_f32_16x16x32_bf16 v[12:15], v[144:147], v[216:219], v[12:15]
	s_setprio 0
	s_setprio 1
	v_mfma_f32_16x16x32_bf16 v[56:59], v[148:151], v[182:185], 0
	v_mfma_f32_16x16x32_bf16 v[52:55], v[156:159], v[182:185], 0
	v_mfma_f32_16x16x32_bf16 v[40:43], v[148:151], v[190:193], 0
	v_mfma_f32_16x16x32_bf16 v[36:39], v[156:159], v[190:193], 0
	v_mfma_f32_16x16x32_bf16 v[24:27], v[148:151], v[198:201], 0
	v_mfma_f32_16x16x32_bf16 v[20:23], v[156:159], v[198:201], 0
	v_mfma_f32_16x16x32_bf16 v[8:11], v[148:151], v[212:215], 0
	v_mfma_f32_16x16x32_bf16 v[4:7], v[156:159], v[212:215], 0
	v_mfma_f32_16x16x32_bf16 v[56:59], v[152:155], v[186:189], v[56:59]
	v_mfma_f32_16x16x32_bf16 v[52:55], v[160:163], v[186:189], v[52:55]
	v_mfma_f32_16x16x32_bf16 v[40:43], v[152:155], v[194:197], v[40:43]
	v_mfma_f32_16x16x32_bf16 v[36:39], v[160:163], v[194:197], v[36:39]
	v_mfma_f32_16x16x32_bf16 v[24:27], v[152:155], v[208:211], v[24:27]
	v_mfma_f32_16x16x32_bf16 v[20:23], v[160:163], v[208:211], v[20:23]
	v_mfma_f32_16x16x32_bf16 v[8:11], v[152:155], v[216:219], v[8:11]
	v_mfma_f32_16x16x32_bf16 v[4:7], v[160:163], v[216:219], v[4:7]
	s_setprio 0
	s_barrier
	s_add_i32 s61, 0, 0x18000
	v_add_u32_e32 v2, s61, v203
	s_add_i32 s63, 0, 0x1c000
	ds_read_b128 v[132:135], v2
	ds_read_b128 v[136:139], v2 offset:1024
	ds_read_b128 v[140:143], v2 offset:2048
	ds_read_b128 v[144:147], v2 offset:3072
	v_add_u32_e32 v2, s63, v203
	ds_read_b128 v[148:151], v2
	ds_read_b128 v[152:155], v2 offset:1024
	ds_read_b128 v[156:159], v2 offset:2048
	ds_read_b128 v[160:163], v2 offset:3072
	s_add_u32 s10, s10, 0x40000
	s_addc_u32 s11, s11, 0
	s_mov_b32 m0, s31
	v_lshl_add_u64 v[236:237], s[10:11], 0, v[164:165]
	ds_read_b128 v[182:185], v206 offset:32768
	ds_read_b128 v[186:189], v206 offset:33792
	ds_read_b128 v[190:193], v206 offset:34816
	ds_read_b128 v[194:197], v206 offset:35840
	ds_read_b128 v[198:201], v206 offset:36864
	ds_read_b128 v[208:211], v206 offset:37888
	ds_read_b128 v[212:215], v206 offset:38912
	ds_read_b128 v[216:219], v206 offset:39936
	global_load_lds_dwordx4 v[236:237], off
	v_lshl_add_u64 v[236:237], s[10:11], 0, v[168:169]
	s_mov_b32 m0, s34
	s_nop 0
	global_load_lds_dwordx4 v[236:237], off
	s_waitcnt vmcnt(8)
	s_waitcnt lgkmcnt(0)
	s_barrier
	s_setprio 1
	s_waitcnt lgkmcnt(0)
	v_mfma_f32_16x16x32_bf16 v[128:131], v[132:135], v[182:185], v[128:131]
	v_mfma_f32_16x16x32_bf16 v[124:127], v[140:143], v[182:185], v[124:127]
	v_mfma_f32_16x16x32_bf16 v[112:115], v[132:135], v[190:193], v[112:115]
	v_mfma_f32_16x16x32_bf16 v[108:111], v[140:143], v[190:193], v[108:111]
	v_mfma_f32_16x16x32_bf16 v[96:99], v[132:135], v[198:201], v[96:99]
	v_mfma_f32_16x16x32_bf16 v[92:95], v[140:143], v[198:201], v[92:95]
	v_mfma_f32_16x16x32_bf16 v[80:83], v[132:135], v[212:215], v[80:83]
	v_mfma_f32_16x16x32_bf16 v[76:79], v[140:143], v[212:215], v[76:79]
	v_mfma_f32_16x16x32_bf16 v[128:131], v[136:139], v[186:189], v[128:131]
	v_mfma_f32_16x16x32_bf16 v[124:127], v[144:147], v[186:189], v[124:127]
	v_mfma_f32_16x16x32_bf16 v[112:115], v[136:139], v[194:197], v[112:115]
	v_mfma_f32_16x16x32_bf16 v[108:111], v[144:147], v[194:197], v[108:111]
	v_mfma_f32_16x16x32_bf16 v[96:99], v[136:139], v[208:211], v[96:99]
	v_mfma_f32_16x16x32_bf16 v[92:95], v[144:147], v[208:211], v[92:95]
	v_mfma_f32_16x16x32_bf16 v[80:83], v[136:139], v[216:219], v[80:83]
	v_mfma_f32_16x16x32_bf16 v[76:79], v[144:147], v[216:219], v[76:79]
	s_setprio 0
	s_setprio 1
	v_mfma_f32_16x16x32_bf16 v[120:123], v[148:151], v[182:185], v[120:123]
	v_mfma_f32_16x16x32_bf16 v[116:119], v[156:159], v[182:185], v[116:119]
	v_mfma_f32_16x16x32_bf16 v[104:107], v[148:151], v[190:193], v[104:107]
	v_mfma_f32_16x16x32_bf16 v[100:103], v[156:159], v[190:193], v[100:103]
	v_mfma_f32_16x16x32_bf16 v[88:91], v[148:151], v[198:201], v[88:91]
	v_mfma_f32_16x16x32_bf16 v[84:87], v[156:159], v[198:201], v[84:87]
	v_mfma_f32_16x16x32_bf16 v[72:75], v[148:151], v[212:215], v[72:75]
	v_mfma_f32_16x16x32_bf16 v[68:71], v[156:159], v[212:215], v[68:71]
	v_mfma_f32_16x16x32_bf16 v[120:123], v[152:155], v[186:189], v[120:123]
	v_mfma_f32_16x16x32_bf16 v[116:119], v[160:163], v[186:189], v[116:119]
	v_mfma_f32_16x16x32_bf16 v[104:107], v[152:155], v[194:197], v[104:107]
	v_mfma_f32_16x16x32_bf16 v[100:103], v[160:163], v[194:197], v[100:103]
	v_mfma_f32_16x16x32_bf16 v[88:91], v[152:155], v[208:211], v[88:91]
	v_mfma_f32_16x16x32_bf16 v[84:87], v[160:163], v[208:211], v[84:87]
	v_mfma_f32_16x16x32_bf16 v[72:75], v[152:155], v[216:219], v[72:75]
	v_mfma_f32_16x16x32_bf16 v[68:71], v[160:163], v[216:219], v[68:71]
	s_setprio 0
	s_barrier
; #define PG8_STAGE(bufoff, gbase, voff) do { _Pragma("unroll") for (int _i = 0; _i < 2; ++_i) \
;         __builtin_amdgcn_global_load_lds((const unsigned*)((const char*)(gbase) + (voff)[_i]), (PG8_LAS unsigned*)(lds + (bufoff) + ldsw + _i * 8192), 16, 0, 0); } while (0)
; #define PG8_LDA(dst, b, h) do { _Pragma("unroll") for (int m = 0; m < 4; ++m) _Pragma("unroll") for (int k = 0; k < 2; ++k) dst[m][k] = *(const PG8_LAS bf16x8*)(lds + PG8_SA(b, h) + aoff + m * 2048 + k * 1024); } while (0)
; #define PG8_MMA(ai, bj, At, Bt) do { __builtin_amdgcn_s_setprio(1); _Pragma("unroll") for (int m = 0; m < 4; ++m) _Pragma("unroll") for (int n = 0; n < 2; ++n) _Pragma("unroll") for (int k = 0; k < 2; ++k) \
;         acc[ai][bj][m][n] = __builtin_amdgcn_mfma_f32_16x16x32_bf16(Bt[n][k], At[m][k], acc[ai][bj][m][n], 0, 0, 0); __builtin_amdgcn_s_setprio(0); } while (0)
; #define PG8_WAIT_V(n) asm volatile("s_waitcnt vmcnt(" #n ")" ::: "memory")
; #define PG8_WAIT_L(n) asm volatile("s_waitcnt lgkmcnt(" #n ")" ::: "memory")
; #define PG8_BAR __builtin_amdgcn_s_barrier()
; #define PG8_SCHED __builtin_amdgcn_sched_barrier(0)
; template <class Epi, class Sched, bool ALIGN_EPI = false, bool SP2 = false>
; __device__ __forceinline__ void gemm_phase(PG8_LAS unsigned char* lds, const Gemm g, const Sched& S, const Epi& E) {
;     ...
;             PG8_LDA(At, 1, 1); PG8_STAGE(PG8_SB(1, 0), b3, voffB); PG8_STAGE(PG8_SB(1, 1), b3 + hstep, voffB); PG8_STAGE(PG8_SA(1, 0), a3, voffA);
;             PG8_WAIT_V(8); PG8_WAIT_L(0); PG8_BAR; if (cur.half == 0) { PG8_MMA(1, 0, At, B0); PG8_MMA(1, 1, At, B1); } PG8_BAR; PG8_SCHED;
	s_add_i32 s10, s61, s27
	v_lshl_add_u64 v[228:229], v[228:229], 0, s[42:43]
	s_mov_b32 m0, s10
	ds_read_b128 v[182:185], v206 offset:49152
	ds_read_b128 v[186:189], v206 offset:50176
	ds_read_b128 v[190:193], v206 offset:51200
	ds_read_b128 v[194:197], v206 offset:52224
	ds_read_b128 v[198:201], v206 offset:53248
	ds_read_b128 v[208:211], v206 offset:54272
	ds_read_b128 v[212:215], v206 offset:55296
	ds_read_b128 v[216:219], v206 offset:56320
	global_load_lds_dwordx4 v[228:229], off
	s_add_i32 m0, s10, 0x2000
	s_add_u32 s0, s0, 0x40080
	v_lshl_add_u64 v[228:229], v[230:231], 0, s[42:43]
	s_addc_u32 s1, s1, 0
	s_add_i32 s10, s63, s27
	global_load_lds_dwordx4 v[228:229], off
	v_lshl_add_u64 v[228:229], s[0:1], 0, v[166:167]
	s_mov_b32 m0, s10
	s_nop 0
	global_load_lds_dwordx4 v[228:229], off
	v_lshl_add_u64 v[228:229], s[0:1], 0, v[170:171]
	s_add_i32 m0, s10, 0x2000
	s_nop 0
	global_load_lds_dwordx4 v[228:229], off
	v_lshl_add_u64 v[228:229], v[232:233], 0, s[42:43]
	s_mov_b32 m0, s41
	s_nop 0
	global_load_lds_dwordx4 v[228:229], off
	v_lshl_add_u64 v[228:229], v[234:235], 0, s[42:43]
	s_mov_b32 m0, s71
	s_nop 0
	global_load_lds_dwordx4 v[228:229], off
	s_waitcnt vmcnt(8)
	s_waitcnt lgkmcnt(0)
	s_barrier
	s_setprio 1
	s_waitcnt lgkmcnt(0)
	v_mfma_f32_16x16x32_bf16 v[64:67], v[132:135], v[182:185], v[64:67]
	v_mfma_f32_16x16x32_bf16 v[60:63], v[140:143], v[182:185], v[60:63]
	v_mfma_f32_16x16x32_bf16 v[48:51], v[132:135], v[190:193], v[48:51]
	v_mfma_f32_16x16x32_bf16 v[44:47], v[140:143], v[190:193], v[44:47]
	v_mfma_f32_16x16x32_bf16 v[32:35], v[132:135], v[198:201], v[32:35]
	v_mfma_f32_16x16x32_bf16 v[28:31], v[140:143], v[198:201], v[28:31]
	v_mfma_f32_16x16x32_bf16 v[16:19], v[132:135], v[212:215], v[16:19]
	v_mfma_f32_16x16x32_bf16 v[12:15], v[140:143], v[212:215], v[12:15]
	v_mfma_f32_16x16x32_bf16 v[64:67], v[136:139], v[186:189], v[64:67]
	v_mfma_f32_16x16x32_bf16 v[60:63], v[144:147], v[186:189], v[60:63]
	v_mfma_f32_16x16x32_bf16 v[48:51], v[136:139], v[194:197], v[48:51]
	v_mfma_f32_16x16x32_bf16 v[44:47], v[144:147], v[194:197], v[44:47]
	v_mfma_f32_16x16x32_bf16 v[32:35], v[136:139], v[208:211], v[32:35]
	v_mfma_f32_16x16x32_bf16 v[28:31], v[144:147], v[208:211], v[28:31]
	v_mfma_f32_16x16x32_bf16 v[16:19], v[136:139], v[216:219], v[16:19]
	v_mfma_f32_16x16x32_bf16 v[12:15], v[144:147], v[216:219], v[12:15]
	s_setprio 0
	s_setprio 1
	v_mfma_f32_16x16x32_bf16 v[56:59], v[148:151], v[182:185], v[56:59]
	v_mfma_f32_16x16x32_bf16 v[52:55], v[156:159], v[182:185], v[52:55]
	v_mfma_f32_16x16x32_bf16 v[40:43], v[148:151], v[190:193], v[40:43]
	v_mfma_f32_16x16x32_bf16 v[36:39], v[156:159], v[190:193], v[36:39]
	v_mfma_f32_16x16x32_bf16 v[24:27], v[148:151], v[198:201], v[24:27]
	v_mfma_f32_16x16x32_bf16 v[20:23], v[156:159], v[198:201], v[20:23]
	v_mfma_f32_16x16x32_bf16 v[8:11], v[148:151], v[212:215], v[8:11]
	v_mfma_f32_16x16x32_bf16 v[4:7], v[156:159], v[212:215], v[4:7]
	v_mfma_f32_16x16x32_bf16 v[56:59], v[152:155], v[186:189], v[56:59]
	v_mfma_f32_16x16x32_bf16 v[52:55], v[160:163], v[186:189], v[52:55]
	v_mfma_f32_16x16x32_bf16 v[40:43], v[152:155], v[194:197], v[40:43]
	v_mfma_f32_16x16x32_bf16 v[36:39], v[160:163], v[194:197], v[36:39]
	v_mfma_f32_16x16x32_bf16 v[24:27], v[152:155], v[208:211], v[24:27]
	v_mfma_f32_16x16x32_bf16 v[20:23], v[160:163], v[208:211], v[20:23]
	v_mfma_f32_16x16x32_bf16 v[8:11], v[152:155], v[216:219], v[8:11]
	v_mfma_f32_16x16x32_bf16 v[4:7], v[160:163], v[216:219], v[4:7]
	s_setprio 0
	s_barrier
	s_add_i32 s39, s39, 2
	s_add_u32 s8, s8, 0x100
	s_addc_u32 s9, s9, 0
	s_add_u32 s36, s36, 0x100
	s_addc_u32 s38, s38, 0

;     __device__ __forceinline__ void a_ready(const Unit&) const { if (++ncall == 3 && sig != nullptr && threadIdx.x == 0) __hip_atomic_fetch_add(sig, 1u, __ATOMIC_RELAXED, __HIP_MEMORY_SCOPE_AGENT); }
;     __device__ bool next(int i, Unit& u) const { if (!base.next(i >> 1, u)) return false; if (i & 1) { u.pm += MTOK / BM; u.pn += DM / BM; } return true; }
; #define PG8_WAIT_V(n) asm volatile("s_waitcnt vmcnt(" #n ")" ::: "memory")
; template <class Epi, class Sched, bool ALIGN_EPI = false, bool SP2 = false>
; __device__ __forceinline__ void gemm_phase(PG8_LAS unsigned char* lds, const Gemm g, const Sched& S, const Epi& E) {
;     ...
;     for (;;) {
;         const bool has_next = S.next(ui + 1, nxt);
;         const char* nA = has_next ? (const char*)g.A + (size_t)nxt.pm * tstep + (nxt.half == 2 ? hstep : (size_t)0) : cA; const char* nB = has_next ? (const char*)g.Bt + (size_t)nxt.pn * tstep : cB;
;         for (int t = 0; t < nt; t += 2) {
;             const bool last = (t == nt - 2);
;             const char* a1 = cA + (size_t)(t + 1) * kstep;
;             const char* a2 = last ? nA : cA + (size_t)(t + 2) * kstep; const char* b2 = last ? nB : cB + (size_t)(t + 2) * kstep;
;             const char* a3 = a2 + kstep; const char* b3 = b2 + kstep;
;             if (last && has_next) S.a_ready(nxt);
;             if constexpr (SP2) {
;             PG8_LDB(B0, 0, 0); PG8_LDB(B1, 0, 1); PG8_SCHED; PG8_LDA(At, 0, 0); PG8_STAGE(PG8_SA(1, 1), a1 + hstep, voffA);
;     ...
;             if (PROBE_KIND == 18 && t == 0 && ui > 0 && g.probe) { const unsigned long long tq_ = __builtin_amdgcn_s_memrealtime(); PG8_WAIT_V(8); pg8_probe_acc += (unsigned)(__builtin_amdgcn_s_memrealtime() - tq_); }
;     ...
;             PG8_WAIT_V(8); PG8_WAIT_L(0); PG8_BAR; PG8_MMA(0, 0, At, B0); PG8_MMA(0, 1, At, B1); PG8_BAR; PG8_SCHED;
;             PG8_LDA(At, 0, 1); PG8_STAGE(PG8_SB(0, 0), b2, voffB); PG8_STAGE(PG8_SB(0, 1), b2 + hstep, voffB); PG8_STAGE(PG8_SA(0, 0), a2, voffA);
;             PG8_WAIT_V(8); PG8_WAIT_L(0); PG8_BAR; if (cur.half == 0) { PG8_MMA(1, 0, At, B0); PG8_MMA(1, 1, At, B1); } PG8_BAR; PG8_SCHED;
;     ...
;         for (int a = 0; a < 2; ++a)
; #pragma unroll
;             for (int b = 0; b < 2; ++b)
; #pragma unroll
;                 for (int m = 0; m < 4; ++m)
; #pragma unroll
;                     for (int n = 0; n < 2; ++n) acc[a][b][m][n] = (f32x4){0.f, 0.f, 0.f, 0.f};
.LBB0_1476:
	s_ashr_i32 s17, s16, 31
	s_lshl_b64 s[28:29], s[16:17], 19
	s_add_u32 s56, s30, s28
	s_addc_u32 s57, s31, s29
	s_and_b64 s[28:29], s[38:39], exec
	s_cselect_b32 s17, s57, s27
	s_cselect_b32 s62, s56, s26
	s_ashr_i32 s19, s18, 31
	s_lshl_b64 s[28:29], s[18:19], 19
	s_add_u32 s58, s34, s28
	s_addc_u32 s59, s35, s29
	s_and_b64 s[28:29], s[38:39], exec
	s_cselect_b32 s19, s59, s1
	s_cselect_b32 s63, s58, s0
	s_add_u32 s26, s26, 0x40080
	s_addc_u32 s27, s27, 0
	s_add_u32 s64, s0, 0x100
	s_addc_u32 s65, s1, 0
	s_mov_b32 s66, -2
	s_add_u32 s0, s26, 0xfffc0080
	s_addc_u32 s1, s27, -1
	s_add_i32 s67, 0, 0x10000
	s_cmp_eq_u32 s66, 12
	s_cselect_b32 s29, s17, s1
	s_cselect_b32 s28, s62, s0
	v_add_u32_e32 v151, s67, v147
	s_cselect_b32 s1, s19, s65
	s_cselect_b32 s0, s63, s64
	s_add_i32 s70, 0, 0x14000
	ds_read_b128 v[142:145], v151
	ds_read_b128 v[152:155], v151 offset:1024
	ds_read_b128 v[156:159], v151 offset:2048
	ds_read_b128 v[160:163], v151 offset:3072
	v_add_u32_e32 v151, s70, v147
	ds_read_b128 v[164:167], v151
	ds_read_b128 v[168:171], v151 offset:1024
	ds_read_b128 v[172:175], v151 offset:2048
	ds_read_b128 v[176:179], v151 offset:3072
	v_lshl_add_u64 v[212:213], s[26:27], 0, v[138:139]
	s_add_i32 m0, s15, 0xc000
	ds_read_b128 v[180:183], v150
	ds_read_b128 v[184:187], v150 offset:1024
	ds_read_b128 v[188:191], v150 offset:2048
	ds_read_b128 v[192:195], v150 offset:3072
	ds_read_b128 v[196:199], v150 offset:4096
	ds_read_b128 v[200:203], v150 offset:5120
	ds_read_b128 v[204:207], v150 offset:6144
	ds_read_b128 v[208:211], v150 offset:7168
	global_load_lds_dwordx4 v[212:213], off
	v_lshl_add_u64 v[212:213], s[26:27], 0, v[140:141]
	s_add_i32 m0, s15, 0xe000
	s_nop 0
	global_load_lds_dwordx4 v[212:213], off
	s_waitcnt vmcnt(8)
	s_waitcnt lgkmcnt(0)
	s_barrier
	s_setprio 1
	s_waitcnt lgkmcnt(0)
	v_mfma_f32_16x16x32_bf16 v[128:131], v[142:145], v[180:183], 0
	v_mfma_f32_16x16x32_bf16 v[124:127], v[156:159], v[180:183], 0
	v_mfma_f32_16x16x32_bf16 v[112:115], v[142:145], v[188:191], 0
	v_mfma_f32_16x16x32_bf16 v[108:111], v[156:159], v[188:191], 0
	v_mfma_f32_16x16x32_bf16 v[96:99], v[142:145], v[196:199], 0
	v_mfma_f32_16x16x32_bf16 v[92:95], v[156:159], v[196:199], 0
	v_mfma_f32_16x16x32_bf16 v[80:83], v[142:145], v[204:207], 0
	v_mfma_f32_16x16x32_bf16 v[76:79], v[156:159], v[204:207], 0
	v_mfma_f32_16x16x32_bf16 v[128:131], v[152:155], v[184:187], v[128:131]
	v_mfma_f32_16x16x32_bf16 v[124:127], v[160:163], v[184:187], v[124:127]
	v_mfma_f32_16x16x32_bf16 v[112:115], v[152:155], v[192:195], v[112:115]
	v_mfma_f32_16x16x32_bf16 v[108:111], v[160:163], v[192:195], v[108:111]
	v_mfma_f32_16x16x32_bf16 v[96:99], v[152:155], v[200:203], v[96:99]
	v_mfma_f32_16x16x32_bf16 v[92:95], v[160:163], v[200:203], v[92:95]
	v_mfma_f32_16x16x32_bf16 v[80:83], v[152:155], v[208:211], v[80:83]
	v_mfma_f32_16x16x32_bf16 v[76:79], v[160:163], v[208:211], v[76:79]
	s_setprio 0
	s_setprio 1
	v_mfma_f32_16x16x32_bf16 v[120:123], v[164:167], v[180:183], 0
	v_mfma_f32_16x16x32_bf16 v[116:119], v[172:175], v[180:183], 0
	v_mfma_f32_16x16x32_bf16 v[104:107], v[164:167], v[188:191], 0
	v_mfma_f32_16x16x32_bf16 v[100:103], v[172:175], v[188:191], 0
	v_mfma_f32_16x16x32_bf16 v[88:91], v[164:167], v[196:199], 0
	v_mfma_f32_16x16x32_bf16 v[84:87], v[172:175], v[196:199], 0
	v_mfma_f32_16x16x32_bf16 v[72:75], v[164:167], v[204:207], 0
	v_mfma_f32_16x16x32_bf16 v[68:71], v[172:175], v[204:207], 0
	v_mfma_f32_16x16x32_bf16 v[120:123], v[168:171], v[184:187], v[120:123]
	v_mfma_f32_16x16x32_bf16 v[116:119], v[176:179], v[184:187], v[116:119]
	v_mfma_f32_16x16x32_bf16 v[104:107], v[168:171], v[192:195], v[104:107]
	v_mfma_f32_16x16x32_bf16 v[100:103], v[176:179], v[192:195], v[100:103]
	v_mfma_f32_16x16x32_bf16 v[88:91], v[168:171], v[200:203], v[88:91]
	v_mfma_f32_16x16x32_bf16 v[84:87], v[176:179], v[200:203], v[84:87]
	v_mfma_f32_16x16x32_bf16 v[72:75], v[168:171], v[208:211], v[72:75]
	v_mfma_f32_16x16x32_bf16 v[68:71], v[176:179], v[208:211], v[68:71]
	s_setprio 0
	s_barrier
	s_add_i32 s67, s67, s25
	v_lshl_add_u64 v[212:213], s[0:1], 0, v[2:3]
	s_mov_b32 m0, s67
	ds_read_b128 v[180:183], v150 offset:16384
	ds_read_b128 v[184:187], v150 offset:17408
	ds_read_b128 v[188:191], v150 offset:18432
	ds_read_b128 v[192:195], v150 offset:19456
	ds_read_b128 v[196:199], v150 offset:20480
	ds_read_b128 v[200:203], v150 offset:21504
	ds_read_b128 v[204:207], v150 offset:22528
	ds_read_b128 v[208:211], v150 offset:23552
	global_load_lds_dwordx4 v[212:213], off
	s_add_i32 m0, s67, 0x2000
	s_add_u32 s68, s0, 0x40000
	v_lshl_add_u64 v[214:215], s[0:1], 0, v[136:137]
	s_addc_u32 s69, s1, 0
	s_add_i32 s67, s70, s25
	global_load_lds_dwordx4 v[214:215], off
	v_lshl_add_u64 v[216:217], s[68:69], 0, v[2:3]
	s_mov_b32 m0, s67
	v_lshl_add_u64 v[218:219], s[28:29], 0, v[134:135]
	global_load_lds_dwordx4 v[216:217], off
	v_lshl_add_u64 v[216:217], s[68:69], 0, v[136:137]
	s_add_i32 m0, s67, 0x2000
	s_nop 0
	global_load_lds_dwordx4 v[216:217], off
	v_lshl_add_u64 v[216:217], s[28:29], 0, v[132:133]
	s_mov_b32 m0, s15
	s_nop 0
	global_load_lds_dwordx4 v[216:217], off
	s_mov_b32 m0, s21
	s_nop 0
	global_load_lds_dwordx4 v[218:219], off
	s_waitcnt vmcnt(8)
	s_waitcnt lgkmcnt(0)
	s_barrier
; #define PG8_STAGE(bufoff, gbase, voff) do { _Pragma("unroll") for (int _i = 0; _i < 2; ++_i) \
;         __builtin_amdgcn_global_load_lds((const unsigned*)((const char*)(gbase) + (voff)[_i]), (PG8_LAS unsigned*)(lds + (bufoff) + ldsw + _i * 8192), 16, 0, 0); } while (0)
; #define PG8_LDA(dst, b, h) do { _Pragma("unroll") for (int m = 0; m < 4; ++m) _Pragma("unroll") for (int k = 0; k < 2; ++k) dst[m][k] = *(const PG8_LAS bf16x8*)(lds + PG8_SA(b, h) + aoff + m * 2048 + k * 1024); } while (0)
; #define PG8_LDB(dst, b, h) do { _Pragma("unroll") for (int n = 0; n < 2; ++n) _Pragma("unroll") for (int k = 0; k < 2; ++k) dst[n][k] = *(const PG8_LAS bf16x8*)(lds + PG8_SB(b, h) + boff + n * 2048 + k * 1024); } while (0)
; #define PG8_MMA(ai, bj, At, Bt) do { __builtin_amdgcn_s_setprio(1); _Pragma("unroll") for (int m = 0; m < 4; ++m) _Pragma("unroll") for (int n = 0; n < 2; ++n) _Pragma("unroll") for (int k = 0; k < 2; ++k) \
;         acc[ai][bj][m][n] = __builtin_amdgcn_mfma_f32_16x16x32_bf16(Bt[n][k], At[m][k], acc[ai][bj][m][n], 0, 0, 0); __builtin_amdgcn_s_setprio(0); } while (0)
; #define PG8_WAIT_V(n) asm volatile("s_waitcnt vmcnt(" #n ")" ::: "memory")
; #define PG8_WAIT_L(n) asm volatile("s_waitcnt lgkmcnt(" #n ")" ::: "memory")
; #define PG8_BAR __builtin_amdgcn_s_barrier()
; #define PG8_SCHED __builtin_amdgcn_sched_barrier(0)
; template <class Epi, class Sched, bool ALIGN_EPI = false, bool SP2 = false>
; __device__ __forceinline__ void gemm_phase(PG8_LAS unsigned char* lds, const Gemm g, const Sched& S, const Epi& E) {
;     ...
;             PG8_WAIT_V(8); PG8_WAIT_L(0); PG8_BAR; if (cur.half == 0) { PG8_MMA(1, 0, At, B0); PG8_MMA(1, 1, At, B1); } PG8_BAR; PG8_SCHED;
;             PG8_LDB(B0, 1, 0); PG8_LDB(B1, 1, 1); PG8_SCHED; PG8_LDA(At, 1, 0); PG8_STAGE(PG8_SA(0, 1), a2 + hstep, voffA);
;             PG8_WAIT_V(8); PG8_WAIT_L(0); PG8_BAR; PG8_MMA(0, 0, At, B0); PG8_MMA(0, 1, At, B1); PG8_BAR; PG8_SCHED;
	s_setprio 1
	s_waitcnt lgkmcnt(0)
	v_mfma_f32_16x16x32_bf16 v[64:67], v[142:145], v[180:183], 0
	v_mfma_f32_16x16x32_bf16 v[60:63], v[156:159], v[180:183], 0
	v_mfma_f32_16x16x32_bf16 v[48:51], v[142:145], v[188:191], 0
	v_mfma_f32_16x16x32_bf16 v[44:47], v[156:159], v[188:191], 0
	v_mfma_f32_16x16x32_bf16 v[32:35], v[142:145], v[196:199], 0
	v_mfma_f32_16x16x32_bf16 v[28:31], v[156:159], v[196:199], 0
	v_mfma_f32_16x16x32_bf16 v[16:19], v[142:145], v[204:207], 0
	v_mfma_f32_16x16x32_bf16 v[12:15], v[156:159], v[204:207], 0
	v_mfma_f32_16x16x32_bf16 v[64:67], v[152:155], v[184:187], v[64:67]
	v_mfma_f32_16x16x32_bf16 v[60:63], v[160:163], v[184:187], v[60:63]
	v_mfma_f32_16x16x32_bf16 v[48:51], v[152:155], v[192:195], v[48:51]
	v_mfma_f32_16x16x32_bf16 v[44:47], v[160:163], v[192:195], v[44:47]
	v_mfma_f32_16x16x32_bf16 v[32:35], v[152:155], v[200:203], v[32:35]
	v_mfma_f32_16x16x32_bf16 v[28:31], v[160:163], v[200:203], v[28:31]
	v_mfma_f32_16x16x32_bf16 v[16:19], v[152:155], v[208:211], v[16:19]
	v_mfma_f32_16x16x32_bf16 v[12:15], v[160:163], v[208:211], v[12:15]
	s_setprio 0
	s_setprio 1
	v_mfma_f32_16x16x32_bf16 v[56:59], v[164:167], v[180:183], 0
	v_mfma_f32_16x16x32_bf16 v[52:55], v[172:175], v[180:183], 0
	v_mfma_f32_16x16x32_bf16 v[40:43], v[164:167], v[188:191], 0
	v_mfma_f32_16x16x32_bf16 v[36:39], v[172:175], v[188:191], 0
	v_mfma_f32_16x16x32_bf16 v[24:27], v[164:167], v[196:199], 0
	v_mfma_f32_16x16x32_bf16 v[20:23], v[172:175], v[196:199], 0
	v_mfma_f32_16x16x32_bf16 v[8:11], v[164:167], v[204:207], 0
	v_mfma_f32_16x16x32_bf16 v[4:7], v[172:175], v[204:207], 0
	v_mfma_f32_16x16x32_bf16 v[56:59], v[168:171], v[184:187], v[56:59]
	v_mfma_f32_16x16x32_bf16 v[52:55], v[176:179], v[184:187], v[52:55]
	v_mfma_f32_16x16x32_bf16 v[40:43], v[168:171], v[192:195], v[40:43]
	v_mfma_f32_16x16x32_bf16 v[36:39], v[176:179], v[192:195], v[36:39]
	v_mfma_f32_16x16x32_bf16 v[24:27], v[168:171], v[200:203], v[24:27]
	v_mfma_f32_16x16x32_bf16 v[20:23], v[176:179], v[200:203], v[20:23]
	v_mfma_f32_16x16x32_bf16 v[8:11], v[168:171], v[208:211], v[8:11]
	v_mfma_f32_16x16x32_bf16 v[4:7], v[176:179], v[208:211], v[4:7]
	s_setprio 0
	s_barrier
	s_add_i32 s67, 0, 0x18000
	v_add_u32_e32 v151, s67, v147
	s_add_i32 s68, 0, 0x1c000
	ds_read_b128 v[142:145], v151
	ds_read_b128 v[152:155], v151 offset:1024
	ds_read_b128 v[156:159], v151 offset:2048
	ds_read_b128 v[160:163], v151 offset:3072
	v_add_u32_e32 v151, s68, v147
	ds_read_b128 v[164:167], v151
	ds_read_b128 v[168:171], v151 offset:1024
	ds_read_b128 v[172:175], v151 offset:2048
	ds_read_b128 v[176:179], v151 offset:3072
	s_add_u32 s28, s28, 0x40000
	s_addc_u32 s29, s29, 0
	s_mov_b32 m0, s36
	v_lshl_add_u64 v[220:221], s[28:29], 0, v[132:133]
	ds_read_b128 v[180:183], v150 offset:32768
	ds_read_b128 v[184:187], v150 offset:33792
	ds_read_b128 v[188:191], v150 offset:34816
	ds_read_b128 v[192:195], v150 offset:35840
	ds_read_b128 v[196:199], v150 offset:36864
	ds_read_b128 v[200:203], v150 offset:37888
	ds_read_b128 v[204:207], v150 offset:38912
	ds_read_b128 v[208:211], v150 offset:39936
	global_load_lds_dwordx4 v[220:221], off
	v_lshl_add_u64 v[220:221], s[28:29], 0, v[134:135]
	s_mov_b32 m0, s40
	s_nop 0
	global_load_lds_dwordx4 v[220:221], off
	s_waitcnt vmcnt(8)
	s_waitcnt lgkmcnt(0)
	s_barrier
	s_setprio 1
	s_waitcnt lgkmcnt(0)
	v_mfma_f32_16x16x32_bf16 v[128:131], v[142:145], v[180:183], v[128:131]
	v_mfma_f32_16x16x32_bf16 v[124:127], v[156:159], v[180:183], v[124:127]
	v_mfma_f32_16x16x32_bf16 v[112:115], v[142:145], v[188:191], v[112:115]
	v_mfma_f32_16x16x32_bf16 v[108:111], v[156:159], v[188:191], v[108:111]
	v_mfma_f32_16x16x32_bf16 v[96:99], v[142:145], v[196:199], v[96:99]
	v_mfma_f32_16x16x32_bf16 v[92:95], v[156:159], v[196:199], v[92:95]
	v_mfma_f32_16x16x32_bf16 v[80:83], v[142:145], v[204:207], v[80:83]
	v_mfma_f32_16x16x32_bf16 v[76:79], v[156:159], v[204:207], v[76:79]
	v_mfma_f32_16x16x32_bf16 v[128:131], v[152:155], v[184:187], v[128:131]
	v_mfma_f32_16x16x32_bf16 v[124:127], v[160:163], v[184:187], v[124:127]
	v_mfma_f32_16x16x32_bf16 v[112:115], v[152:155], v[192:195], v[112:115]
	v_mfma_f32_16x16x32_bf16 v[108:111], v[160:163], v[192:195], v[108:111]
	v_mfma_f32_16x16x32_bf16 v[96:99], v[152:155], v[200:203], v[96:99]
	v_mfma_f32_16x16x32_bf16 v[92:95], v[160:163], v[200:203], v[92:95]
	v_mfma_f32_16x16x32_bf16 v[80:83], v[152:155], v[208:211], v[80:83]
	v_mfma_f32_16x16x32_bf16 v[76:79], v[160:163], v[208:211], v[76:79]
	s_setprio 0
	s_setprio 1
	v_mfma_f32_16x16x32_bf16 v[120:123], v[164:167], v[180:183], v[120:123]
	v_mfma_f32_16x16x32_bf16 v[116:119], v[172:175], v[180:183], v[116:119]
	v_mfma_f32_16x16x32_bf16 v[104:107], v[164:167], v[188:191], v[104:107]
	v_mfma_f32_16x16x32_bf16 v[100:103], v[172:175], v[188:191], v[100:103]
	v_mfma_f32_16x16x32_bf16 v[88:91], v[164:167], v[196:199], v[88:91]
	v_mfma_f32_16x16x32_bf16 v[84:87], v[172:175], v[196:199], v[84:87]
	v_mfma_f32_16x16x32_bf16 v[72:75], v[164:167], v[204:207], v[72:75]
	v_mfma_f32_16x16x32_bf16 v[68:71], v[172:175], v[204:207], v[68:71]
	v_mfma_f32_16x16x32_bf16 v[120:123], v[168:171], v[184:187], v[120:123]
	v_mfma_f32_16x16x32_bf16 v[116:119], v[176:179], v[184:187], v[116:119]
	v_mfma_f32_16x16x32_bf16 v[104:107], v[168:171], v[192:195], v[104:107]
	v_mfma_f32_16x16x32_bf16 v[100:103], v[176:179], v[192:195], v[100:103]
	v_mfma_f32_16x16x32_bf16 v[88:91], v[168:171], v[200:203], v[88:91]
	v_mfma_f32_16x16x32_bf16 v[84:87], v[176:179], v[200:203], v[84:87]
	v_mfma_f32_16x16x32_bf16 v[72:75], v[168:171], v[208:211], v[72:75]
	v_mfma_f32_16x16x32_bf16 v[68:71], v[176:179], v[208:211], v[68:71]
	s_setprio 0
	s_barrier
; #define PG8_STAGE(bufoff, gbase, voff) do { _Pragma("unroll") for (int _i = 0; _i < 2; ++_i) \
;         __builtin_amdgcn_global_load_lds((const unsigned*)((const char*)(gbase) + (voff)[_i]), (PG8_LAS unsigned*)(lds + (bufoff) + ldsw + _i * 8192), 16, 0, 0); } while (0)
; #define PG8_LDA(dst, b, h) do { _Pragma("unroll") for (int m = 0; m < 4; ++m) _Pragma("unroll") for (int k = 0; k < 2; ++k) dst[m][k] = *(const PG8_LAS bf16x8*)(lds + PG8_SA(b, h) + aoff + m * 2048 + k * 1024); } while (0)
; #define PG8_MMA(ai, bj, At, Bt) do { __builtin_amdgcn_s_setprio(1); _Pragma("unroll") for (int m = 0; m < 4; ++m) _Pragma("unroll") for (int n = 0; n < 2; ++n) _Pragma("unroll") for (int k = 0; k < 2; ++k) \
;         acc[ai][bj][m][n] = __builtin_amdgcn_mfma_f32_16x16x32_bf16(Bt[n][k], At[m][k], acc[ai][bj][m][n], 0, 0, 0); __builtin_amdgcn_s_setprio(0); } while (0)
; #define PG8_WAIT_V(n) asm volatile("s_waitcnt vmcnt(" #n ")" ::: "memory")
; #define PG8_WAIT_L(n) asm volatile("s_waitcnt lgkmcnt(" #n ")" ::: "memory")
; #define PG8_BAR __builtin_amdgcn_s_barrier()
; #define PG8_SCHED __builtin_amdgcn_sched_barrier(0)
; template <class Epi, class Sched, bool ALIGN_EPI = false, bool SP2 = false>
; __device__ __forceinline__ void gemm_phase(PG8_LAS unsigned char* lds, const Gemm g, const Sched& S, const Epi& E) {
;     ...
;             PG8_LDA(At, 1, 1); PG8_STAGE(PG8_SB(1, 0), b3, voffB); PG8_STAGE(PG8_SB(1, 1), b3 + hstep, voffB); PG8_STAGE(PG8_SA(1, 0), a3, voffA);
;             PG8_WAIT_V(8); PG8_WAIT_L(0); PG8_BAR; if (cur.half == 0) { PG8_MMA(1, 0, At, B0); PG8_MMA(1, 1, At, B1); } PG8_BAR; PG8_SCHED;
	s_add_i32 s28, s67, s25
	v_lshl_add_u64 v[212:213], v[212:213], 0, s[42:43]
	s_mov_b32 m0, s28
	ds_read_b128 v[180:183], v150 offset:49152
	ds_read_b128 v[184:187], v150 offset:50176
	ds_read_b128 v[188:191], v150 offset:51200
	ds_read_b128 v[192:195], v150 offset:52224
	ds_read_b128 v[196:199], v150 offset:53248
	ds_read_b128 v[200:203], v150 offset:54272
	ds_read_b128 v[204:207], v150 offset:55296
	ds_read_b128 v[208:211], v150 offset:56320
	global_load_lds_dwordx4 v[212:213], off
	s_add_i32 m0, s28, 0x2000
	s_add_u32 s0, s0, 0x40080
	v_lshl_add_u64 v[212:213], v[214:215], 0, s[42:43]
	s_addc_u32 s1, s1, 0
	s_add_i32 s28, s68, s25
	global_load_lds_dwordx4 v[212:213], off
	v_lshl_add_u64 v[212:213], s[0:1], 0, v[2:3]
	s_mov_b32 m0, s28
	s_nop 0
	global_load_lds_dwordx4 v[212:213], off
	v_lshl_add_u64 v[212:213], s[0:1], 0, v[136:137]
	s_add_i32 m0, s28, 0x2000
	s_nop 0
	global_load_lds_dwordx4 v[212:213], off
	v_lshl_add_u64 v[212:213], v[216:217], 0, s[42:43]
	s_mov_b32 m0, s41
	s_nop 0
	global_load_lds_dwordx4 v[212:213], off
	v_lshl_add_u64 v[212:213], v[218:219], 0, s[42:43]
	s_mov_b32 m0, s60
	s_nop 0
	global_load_lds_dwordx4 v[212:213], off
	s_waitcnt vmcnt(8)
	s_waitcnt lgkmcnt(0)
	s_barrier
	s_setprio 1
	s_waitcnt lgkmcnt(0)
	v_mfma_f32_16x16x32_bf16 v[64:67], v[142:145], v[180:183], v[64:67]
	v_mfma_f32_16x16x32_bf16 v[60:63], v[156:159], v[180:183], v[60:63]
	v_mfma_f32_16x16x32_bf16 v[48:51], v[142:145], v[188:191], v[48:51]
	v_mfma_f32_16x16x32_bf16 v[44:47], v[156:159], v[188:191], v[44:47]
	v_mfma_f32_16x16x32_bf16 v[32:35], v[142:145], v[196:199], v[32:35]
	v_mfma_f32_16x16x32_bf16 v[28:31], v[156:159], v[196:199], v[28:31]
	v_mfma_f32_16x16x32_bf16 v[16:19], v[142:145], v[204:207], v[16:19]
	v_mfma_f32_16x16x32_bf16 v[12:15], v[156:159], v[204:207], v[12:15]
	v_mfma_f32_16x16x32_bf16 v[64:67], v[152:155], v[184:187], v[64:67]
	v_mfma_f32_16x16x32_bf16 v[60:63], v[160:163], v[184:187], v[60:63]
	v_mfma_f32_16x16x32_bf16 v[48:51], v[152:155], v[192:195], v[48:51]
	v_mfma_f32_16x16x32_bf16 v[44:47], v[160:163], v[192:195], v[44:47]
	v_mfma_f32_16x16x32_bf16 v[32:35], v[152:155], v[200:203], v[32:35]
	v_mfma_f32_16x16x32_bf16 v[28:31], v[160:163], v[200:203], v[28:31]
	v_mfma_f32_16x16x32_bf16 v[16:19], v[152:155], v[208:211], v[16:19]
	v_mfma_f32_16x16x32_bf16 v[12:15], v[160:163], v[208:211], v[12:15]
	s_setprio 0
	s_setprio 1
	v_mfma_f32_16x16x32_bf16 v[56:59], v[164:167], v[180:183], v[56:59]
	v_mfma_f32_16x16x32_bf16 v[52:55], v[172:175], v[180:183], v[52:55]
	v_mfma_f32_16x16x32_bf16 v[40:43], v[164:167], v[188:191], v[40:43]
	v_mfma_f32_16x16x32_bf16 v[36:39], v[172:175], v[188:191], v[36:39]
	v_mfma_f32_16x16x32_bf16 v[24:27], v[164:167], v[196:199], v[24:27]
	v_mfma_f32_16x16x32_bf16 v[20:23], v[172:175], v[196:199], v[20:23]
	v_mfma_f32_16x16x32_bf16 v[8:11], v[164:167], v[204:207], v[8:11]
	v_mfma_f32_16x16x32_bf16 v[4:7], v[172:175], v[204:207], v[4:7]
	v_mfma_f32_16x16x32_bf16 v[56:59], v[168:171], v[184:187], v[56:59]
	v_mfma_f32_16x16x32_bf16 v[52:55], v[176:179], v[184:187], v[52:55]
	v_mfma_f32_16x16x32_bf16 v[40:43], v[168:171], v[192:195], v[40:43]
	v_mfma_f32_16x16x32_bf16 v[36:39], v[176:179], v[192:195], v[36:39]
	v_mfma_f32_16x16x32_bf16 v[24:27], v[168:171], v[200:203], v[24:27]
	v_mfma_f32_16x16x32_bf16 v[20:23], v[176:179], v[200:203], v[20:23]
	v_mfma_f32_16x16x32_bf16 v[8:11], v[168:171], v[208:211], v[8:11]
	v_mfma_f32_16x16x32_bf16 v[4:7], v[176:179], v[208:211], v[4:7]
	s_setprio 0
	s_barrier
	s_add_i32 s66, s66, 2
	s_add_u32 s26, s26, 0x100
	s_addc_u32 s27, s27, 0
	s_add_u32 s64, s64, 0x100
	s_addc_u32 s65, s65, 0
